# v57 + stage B: lru_B chains moved to workgroups 252-255 so they overlap ssd_B (WGs 0-127) instead of serializing after it
# speedup vs baseline: 1.0016x; 1.0016x over previous
.LBB0_791:
	s_or_b64 exec, exec, s[0:1]
	s_movk_i32 s0, 0x800
	s_mov_b32 s39, s63
	v_xor_b32_e32 v1, 0x1fe00, v1
	v_cmp_gt_i32_e32 vcc, s0, v1
	s_and_saveexec_b64 s[0:1], vcc
	s_mov_b32 s15, 0x26000
	s_mov_b32 s16, 0x28000
	s_mov_b32 s17, 0x2a000
	s_mov_b32 s21, 0x2c000
	s_mov_b32 s22, 0x2e000
	s_mov_b32 s24, 0x30000
	s_mov_b32 s25, 0x32000
	s_mov_b32 s85, 0x34000
	s_mov_b32 s93, 0x36000
	s_mov_b32 s96, 0x38000
	s_mov_b32 s97, 0x3a000
	s_mov_b32 s12, 0x3c000
	s_mov_b32 s69, 0x3e000
	s_movk_i32 s41, 0x7ff
	s_cbranch_execz .LBB0_794
	s_ashr_i32 s4, s14, 31
	s_add_u32 s8, s36, s14
	v_readlane_b32 s6, v254, 6
	s_addc_u32 s9, s37, s4
	v_readlane_b32 s7, v254, 7
	s_add_u32 s4, s8, 0xb00000
	s_load_dword s10, s[6:7], 0x0
	s_addc_u32 s5, s9, 0
	s_add_u32 s6, s8, 0xa00000
	s_addc_u32 s7, s9, 0
	s_add_u32 s8, s8, 0xc00000
	s_addc_u32 s9, s9, 0
	s_waitcnt lgkmcnt(0)
	s_lshl_b32 s14, s10, 9
	s_mov_b64 s[10:11], 0
